# QKV: bias->LDS copy rewritten as 5 straight-line loads with one wait (was 3 serialized load/wait rounds)
# speedup vs baseline: 1.0115x; 1.0010x over previous
_Z9k_gemm192IN4g1926EpiQKVEEvNS0_4GemmET_:
	s_load_dwordx4 s[4:7], s[0:1], 0x10
	s_load_dword s24, s[0:1], 0x20
	s_load_dword s3, s[0:1], 0x48
	v_mov_b32_e32 v2, v0
	s_waitcnt lgkmcnt(0)
	s_load_dwordx2 s[10:11], s[0:1], 0x40
	v_lshlrev_b32_e32 v1, 2, v0
	v_add_u32_e32 v3, 0x1000, v1
	v_add_u32_e32 v9, 0x1e000, v1
	v_cmp_gt_u32_e32 vcc, 0x100, v0
	s_waitcnt lgkmcnt(0)
	global_load_dword v4, v1, s[10:11]
	global_load_dword v5, v1, s[10:11] offset:2048
	global_load_dword v6, v3, s[10:11]
	global_load_dword v7, v3, s[10:11] offset:2048
	s_and_saveexec_b64 s[8:9], vcc
	s_cbranch_execz .Lqb_skip
	v_add_u32_e32 v3, 0x2000, v1
	global_load_dword v8, v3, s[10:11]
	s_waitcnt vmcnt(0)
	ds_write_b32 v9, v8 offset:8192
.Lqb_skip:
	s_or_b64 exec, exec, s[8:9]
	s_waitcnt vmcnt(0)
	ds_write_b32 v9, v4
	ds_write_b32 v9, v5 offset:2048
	ds_write_b32 v9, v6 offset:4096
	ds_write_b32 v9, v7 offset:6144
	s_ashr_i32 s8, s4, 31
	s_lshr_b32 s8, s8, 25
	s_add_i32 s4, s4, s8
	s_ashr_i32 s28, s4, 7
	s_mul_hi_i32 s4, s5, 0x2aaaaaab
	s_lshr_b32 s5, s4, 31
	s_ashr_i32 s16, s4, 5
	s_add_i32 s16, s16, s5
	s_mul_i32 s4, s16, s28
	s_cmp_ge_i32 s2, s4
	v_readfirstlane_b32 s29, v0
	s_waitcnt lgkmcnt(0)
	s_barrier
	s_cbranch_scc1 .LBB3_38
	s_ashr_i32 s5, s4, 31
	s_lshr_b32 s8, s5, 29
	s_add_i32 s8, s4, s8
	s_ashr_i32 s30, s8, 3
	s_and_b32 s8, s8, -8
	s_ashr_i32 s33, s2, 31
	s_sub_i32 s31, s4, s8
	s_lshr_b32 s8, s33, 29
	s_add_i32 s11, s2, s8
	s_and_b32 s8, s11, -8
	s_sub_i32 s10, s2, s8
	s_add_i32 s34, s30, 1
	s_cmp_ge_i32 s10, s31
	s_mul_i32 s35, s34, s31
	s_cbranch_scc0 .LBB3_16
	s_sub_i32 s8, s10, s31
	s_mul_i32 s8, s8, s30
	s_add_i32 s17, s8, s35
	s_load_dwordx4 s[12:15], s[0:1], 0x0
	s_ashr_i32 s18, s11, 3
	s_cbranch_execz .LBB3_17
	s_branch .LBB3_18
